# v36 with the instruction stream shifted by 16 bytes (4 s_nop at entry): code-placement check
# speedup vs baseline: 1.0055x; 1.0055x over previous
_Z3fwd4Args:
	s_nop 0
	s_nop 0
	s_nop 0
	s_nop 0
	s_load_dword s72, s[0:1], 0xe8
	s_load_dwordx2 s[8:9], s[0:1], 0xe0
	s_load_dwordx8 s[64:71], s[0:1], 0xc0
	s_mov_b32 s96, s2
	s_add_u32 s2, s0, 0xe8
	s_addc_u32 s3, s1, 0
	v_readfirstlane_b32 s10, v0
	v_writelane_b32 v255, s2, 0
	s_mov_b32 s97, 0
	v_cmp_eq_u32_e32 vcc, 0, v0
	v_writelane_b32 v255, s3, 1
	s_waitcnt lgkmcnt(0)
	s_sub_i32 s2, s9, s8
	s_cmp_lt_i32 s2, 2
	s_cbranch_scc1 .LBB0_5
	s_getreg_b32 s2, hwreg(HW_REG_XCC_ID, 0, 4)
	s_and_b32 s97, s2, 15
	s_and_saveexec_b64 s[2:3], vcc
	s_cbranch_execz .LBB0_4
	s_mov_b64 s[4:5], exec
	v_mbcnt_lo_u32_b32 v1, s4, 0
	v_mbcnt_hi_u32_b32 v1, s5, v1
	v_cmp_eq_u32_e32 vcc, 0, v1
	s_and_b64 s[6:7], exec, vcc
	s_mov_b64 exec, s[6:7]
	s_cbranch_execz .LBB0_4
	s_lshl_b32 s6, s97, 8
	s_bcnt1_i32_b64 s4, s[4:5]
	v_mov_b32_e32 v1, s6
	v_mov_b32_e32 v2, s4
	global_atomic_add v1, v2, s[70:71] offset:1024
